# speedup vs baseline: 1.0969x; 1.0042x over previous
.LBB0_20:
	v_lshrrev_b32_e32 v2, 4, v120
	v_lshl_add_u32 v3, v123, 4, v131
	v_lshl_add_u32 v3, v2, 2, v3
	v_lshlrev_b32_e32 v2, 4, v123
	ds_write2st64_b32 v3, v94, v95 offset0:76 offset1:77
	ds_write2st64_b32 v3, v98, v99 offset0:78 offset1:79
	ds_write2st64_b32 v3, v100, v101 offset0:80 offset1:81
	ds_write2st64_b32 v3, v102, v103 offset0:82 offset1:83
	ds_write2st64_b32 v3, v104, v105 offset0:84 offset1:85
	ds_write2st64_b32 v3, v106, v107 offset0:86 offset1:87
	ds_write2st64_b32 v3, v108, v109 offset0:88 offset1:89
	ds_write2st64_b32 v3, v110, v111 offset0:90 offset1:91
	ds_write2st64_b32 v3, v112, v113 offset0:92 offset1:93
	ds_write2st64_b32 v3, v114, v115 offset0:94 offset1:95
	ds_write2st64_b32 v3, v116, v117 offset0:96 offset1:97
	v_mov_b32_e32 v3, 0
	s_waitcnt lgkmcnt(0)
	s_barrier
	s_and_saveexec_b64 s[4:5], s[0:1]
	s_cbranch_execz .LBB0_22
	v_lshlrev_b32_e32 v8, 1, v121
	v_lshrrev_b32_e32 v3, 4, v122
	v_or_b32_e32 v3, v8, v3
	v_lshl_or_b32 v9, v3, 8, v2
	v_add_u32_e32 v4, 0x4c00, v9
	v_add_u32_e32 v5, 0xe400, v9
	ds_read_b128 v[10:13], v4
	ds_read_b128 v[14:17], v4 offset:9728
	ds_read_b128 v[18:21], v4 offset:19456
	ds_read_b128 v[22:25], v4 offset:29184
	ds_read_b128 v[26:29], v5
	ds_read_b128 v[30:33], v5 offset:9728
	ds_read_b128 v[34:37], v5 offset:19456
	ds_read_b128 v[38:41], v5 offset:29184
	v_sub_u32_e32 v4, 11, v8
	v_cvt_f32_i32_e32 v4, v4
	v_cmp_lt_u32_e32 vcc, 31, v0
	v_mul_f32_e32 v3, 0xbf38aa3b, v4
	v_mul_f32_e32 v3, v3, v4
	v_exp_f32_e32 v3, v3
	s_nop 0
	v_cndmask_b32_e32 v46, 1.0, v3, vcc
	s_waitcnt lgkmcnt(4)
	v_add_f32_e32 v10, v10, v11
	v_add_f32_e32 v12, v12, v13
	v_add_f32_e32 v14, v14, v15
	v_add_f32_e32 v16, v16, v17
	v_add_f32_e32 v18, v18, v19
	v_add_f32_e32 v20, v20, v21
	v_add_f32_e32 v22, v22, v23
	v_add_f32_e32 v24, v24, v25
	v_add_f32_e32 v10, v10, v12
	v_add_f32_e32 v14, v14, v16
	v_add_f32_e32 v18, v18, v20
	v_add_f32_e32 v22, v22, v24
	v_add_f32_e32 v10, v10, v14
	v_add_f32_e32 v18, v18, v22
	v_add_f32_e32 v10, v10, v18
	s_waitcnt lgkmcnt(0)
	v_add_f32_e32 v26, v26, v27
	v_add_f32_e32 v28, v28, v29
	v_add_f32_e32 v30, v30, v31
	v_add_f32_e32 v32, v32, v33
	v_add_f32_e32 v34, v34, v35
	v_add_f32_e32 v36, v36, v37
	v_add_f32_e32 v38, v38, v39
	v_add_f32_e32 v40, v40, v41
	v_add_f32_e32 v26, v26, v28
	v_add_f32_e32 v30, v30, v32
	v_add_f32_e32 v34, v34, v36
	v_add_f32_e32 v38, v38, v40
	v_add_f32_e32 v26, v26, v30
	v_add_f32_e32 v34, v34, v38
	v_add_f32_e32 v26, v26, v34
	v_add_f32_e32 v2, v10, v26
	v_mul_f32_e32 v2, v46, v2
	v_max_f32_e32 v2, 0x2edbe6ff, v2
	v_log_f32_e32 v2, v2
	v_cmp_lt_i32_e32 vcc, 1, v119
	v_mul_f32_e32 v2, v118, v2
	s_nop 0
	v_cndmask_b32_e32 v3, 0, v2, vcc

.LBB0_24:
	s_or_b64 exec, exec, s[0:1]
	v_cmp_eq_u32_e32 vcc, 0, v0
	s_waitcnt lgkmcnt(0)
	s_barrier
	s_and_saveexec_b64 s[0:1], vcc
	s_cbranch_execz .LBB0_26
	v_mov_b32_e32 v0, 0x18000
	ds_read_b128 v[0:3], v0
	v_mov_b32_e32 v4, 0x18010
	ds_read_b128 v[4:7], v4
	s_ashr_i32 s3, s2, 31
	s_lshl_b64 s[0:1], s[2:3], 2
	s_waitcnt lgkmcnt(0)
	v_add_f32_e32 v0, v0, v1
	v_add_f32_e32 v2, v2, v3
	v_add_f32_e32 v4, v4, v5
	v_add_f32_e32 v6, v6, v7
	v_add_f32_e32 v0, v0, v2
	v_add_f32_e32 v4, v4, v6
	v_add_f32_e32 v0, v0, v4
	s_add_u32 s0, s14, s0
	v_mul_f32_e32 v0, 0x3be32166, v0
	s_addc_u32 s1, s15, s1
	v_mov_b32_e32 v1, 0
	global_store_dword v1, v0, s[0:1]
